# PEER table f32 row loads (read once) tagged nt so they do not displace the GEMM panels in L2/MALL
# speedup vs baseline: 1.0072x; 1.0072x over previous
; __device__ __forceinline__ void pt_load(const float* tu, const float* tv, f32x4* v, int r, int lane) {
;     const f32x4* sp = (const f32x4*)(((r >> 14) ? tv : tu) + (size_t)(r & 16383) * D) + lane;
; #pragma unroll
;     for (int j = 0; j < 16; ++j) v[j] = sp[64 * j];
; }
; __device__ __forceinline__ void pt_proc(unsigned char* PT, const f32x4* v, int r, int lane) {
;     const int tb = r >> 14, e = r & 16383; unsigned char* tab = PT + (tb ? PT_V8 : 0); float amax = 0.f;
; #pragma unroll
;     for (int j = 0; j < 16; ++j) amax = fmaxf(fmaxf(amax, fmaxf(fabsf(v[j].x), fabsf(v[j].y))), fmaxf(fabsf(v[j].z), fabsf(v[j].w)));
.LBB0_202:
	s_and_b32 s10, s25, 0x3fff000
	s_add_i32 s30, s66, s23
	s_lshl_b32 s36, s10, 2
	s_cmpk_lt_u32 s30, 0x4000
	s_cselect_b64 s[10:11], -1, 0
	s_and_b64 s[34:35], s[10:11], exec
	s_cselect_b32 s34, s12, s14
	s_cselect_b32 s35, s13, s15
	s_cselect_b32 s31, 0, 0x4000000
	s_add_u32 s34, s34, s36
	s_addc_u32 s35, s35, 0
	v_lshlrev_b32_e32 v204, 4, v194
	s_movk_i32 s36, 0x2000
	v_lshl_add_u64 v[2:3], s[34:35], 0, v[204:205]
	v_add_co_u32_e32 v4, vcc, s36, v2
	global_load_dwordx4 v[68:71], v204, s[34:35] nt
	global_load_dwordx4 v[72:75], v204, s[34:35] offset:1024 nt
	global_load_dwordx4 v[54:57], v204, s[34:35] offset:2048 nt
	global_load_dwordx4 v[50:53], v204, s[34:35] offset:3072 nt
	v_addc_co_u32_e32 v5, vcc, 0, v3, vcc
	global_load_dwordx4 v[46:49], v[4:5], off offset:-4096 nt
	s_movk_i32 s37, 0x1000
	v_add_co_u32_e32 v6, vcc, s37, v2
	s_movk_i32 s34, 0x3000
	s_nop 0
	v_addc_co_u32_e32 v7, vcc, 0, v3, vcc
	global_load_dwordx4 v[42:45], v[6:7], off offset:1024 nt
	global_load_dwordx4 v[38:41], v[6:7], off offset:2048 nt
	global_load_dwordx4 v[34:37], v[6:7], off offset:3072 nt
	global_load_dwordx4 v[30:33], v[4:5], off nt
	global_load_dwordx4 v[26:29], v[4:5], off offset:1024 nt
	global_load_dwordx4 v[22:25], v[4:5], off offset:2048 nt
	v_add_co_u32_e32 v2, vcc, s34, v2
	v_lshlrev_b32_e32 v204, 2, v194
	s_nop 0
	v_addc_co_u32_e32 v3, vcc, 0, v3, vcc
	global_load_dwordx4 v[18:21], v[4:5], off offset:3072 nt
	global_load_dwordx4 v[14:17], v[2:3], off nt
	global_load_dwordx4 v[10:13], v[2:3], off offset:1024 nt
	global_load_dwordx4 v[6:9], v[2:3], off offset:2048 nt
	s_nop 0
	global_load_dwordx4 v[2:5], v[2:3], off offset:3072 nt
	global_load_dword v247, v204, s[12:13]
	global_load_dword v247, v204, s[12:13]
	global_load_dword v247, v204, s[12:13]
	global_load_dword v247, v204, s[12:13]
	global_load_dword v247, v204, s[12:13]
	global_load_dword v247, v204, s[12:13]
	global_load_dword v247, v204, s[12:13]
	global_load_dword v247, v204, s[12:13]
	global_load_dword v247, v204, s[12:13]
	global_load_dword v247, v204, s[12:13]
	global_load_dword v247, v204, s[12:13]
	global_load_dword v247, v204, s[12:13]
	global_load_dword v247, v204, s[12:13]
	global_load_dword v247, v204, s[12:13]
	global_load_dword v247, v204, s[12:13]
	global_load_dword v247, v204, s[12:13]
	global_load_dword v247, v204, s[12:13]
.Lside_loop:
	s_add_i32 s23, s23, 8
	s_add_i32 s25, s25, 0x8000
	s_and_b32 s38, s25, 0x3fff000
	s_add_i32 s40, s66, s23
	s_lshl_b32 s36, s38, 2
	s_cmpk_lt_u32 s40, 0x4000
	s_cselect_b64 s[38:39], -1, 0
	s_and_b64 s[34:35], s[38:39], exec
	s_cselect_b32 s34, s12, s14
	s_cselect_b32 s35, s13, s15
	s_cselect_b32 s41, 0, 0x4000000
	s_add_u32 s34, s34, s36
	s_addc_u32 s35, s35, 0
	v_lshlrev_b32_e32 v204, 4, v194
	s_movk_i32 s36, 0x2000
	v_lshl_add_u64 v[136:137], s[34:35], 0, v[204:205]
	v_add_co_u32_e32 v138, vcc, s36, v136
	global_load_dwordx4 v[216:219], v204, s[34:35] nt
	global_load_dwordx4 v[220:223], v204, s[34:35] offset:1024 nt
	global_load_dwordx4 v[188:191], v204, s[34:35] offset:2048 nt
	global_load_dwordx4 v[184:187], v204, s[34:35] offset:3072 nt
	v_addc_co_u32_e32 v139, vcc, 0, v137, vcc
	global_load_dwordx4 v[180:183], v[138:139], off offset:-4096 nt
	s_movk_i32 s37, 0x1000
	v_add_co_u32_e32 v140, vcc, s37, v136
	s_movk_i32 s34, 0x3000
	s_nop 0
	v_addc_co_u32_e32 v141, vcc, 0, v137, vcc
	global_load_dwordx4 v[176:179], v[140:141], off offset:1024 nt
	global_load_dwordx4 v[172:175], v[140:141], off offset:2048 nt
	global_load_dwordx4 v[168:171], v[140:141], off offset:3072 nt
	global_load_dwordx4 v[164:167], v[138:139], off nt
	global_load_dwordx4 v[160:163], v[138:139], off offset:1024 nt
	global_load_dwordx4 v[156:159], v[138:139], off offset:2048 nt
	v_add_co_u32_e32 v136, vcc, s34, v136
	v_lshlrev_b32_e32 v204, 2, v194
	s_nop 0
	v_addc_co_u32_e32 v137, vcc, 0, v137, vcc
	global_load_dwordx4 v[152:155], v[138:139], off offset:3072 nt
	global_load_dwordx4 v[148:151], v[136:137], off nt
	global_load_dwordx4 v[144:147], v[136:137], off offset:1024 nt
	global_load_dwordx4 v[140:143], v[136:137], off offset:2048 nt
	s_nop 0
	global_load_dwordx4 v[136:139], v[136:137], off offset:3072 nt
	s_waitcnt vmcnt(48)
	v_max_f32_e64 v58, |v69|, |v69|
	v_max_f32_e64 v59, |v68|, |v68|
	v_max_f32_e64 v66, |v71|, |v71|
	v_max_f32_e64 v67, |v70|, |v70|
	s_waitcnt vmcnt(47)
	v_max_f32_e64 v76, |v73|, |v73|
	v_max_f32_e64 v77, |v72|, |v72|
	v_max_f32_e64 v78, |v75|, |v75|
	v_max_f32_e64 v79, |v74|, |v74|
	v_max_f32_e32 v58, v59, v58
	v_max_f32_e32 v59, v67, v66
	s_waitcnt vmcnt(46)
	v_max_f32_e64 v80, |v55|, |v55|
	v_max_f32_e64 v81, |v54|, |v54|
	v_max_f32_e64 v82, |v57|, |v57|
	v_max_f32_e64 v83, |v56|, |v56|
	v_max_f32_e32 v66, v77, v76
	v_max_f32_e32 v67, v79, v78
	v_max3_f32 v58, v58, 0, v59
	s_waitcnt vmcnt(45)
	v_max_f32_e64 v84, |v51|, |v51|
	v_max_f32_e64 v85, |v50|, |v50|
	v_max_f32_e64 v86, |v53|, |v53|
	v_max_f32_e64 v87, |v52|, |v52|
	v_max_f32_e32 v76, v81, v80
	v_max_f32_e32 v77, v83, v82
	v_max3_f32 v58, v58, v66, v67
	v_max_f32_e32 v78, v85, v84
	v_max_f32_e32 v79, v87, v86
	s_waitcnt vmcnt(44)
	v_max_f32_e64 v59, |v47|, |v47|
	v_max_f32_e64 v80, |v46|, |v46|
	v_max_f32_e64 v81, |v49|, |v49|
	v_max_f32_e64 v82, |v48|, |v48|
	v_max3_f32 v58, v58, v76, v77
	s_waitcnt vmcnt(43)
	v_max_f32_e64 v83, |v43|, |v43|
	v_max_f32_e64 v84, |v42|, |v42|
	v_max_f32_e64 v85, |v45|, |v45|
	v_max_f32_e64 v86, |v44|, |v44|
	v_max_f32_e32 v59, v80, v59
	v_max_f32_e32 v66, v82, v81
	v_max3_f32 v58, v58, v78, v79
	s_waitcnt vmcnt(42)
	v_max_f32_e64 v87, |v39|, |v39|
	v_max_f32_e64 v88, |v38|, |v38|
	v_max_f32_e64 v89, |v41|, |v41|
	v_max_f32_e64 v90, |v40|, |v40|
	v_max_f32_e32 v67, v84, v83
	v_max_f32_e32 v80, v86, v85
	v_max3_f32 v58, v58, v59, v66
	s_waitcnt vmcnt(41)
; __device__ __forceinline__ void pt_proc(unsigned char* PT, const f32x4* v, int r, int lane) {
;     const int tb = r >> 14, e = r & 16383; unsigned char* tab = PT + (tb ? PT_V8 : 0); float amax = 0.f;
; #pragma unroll
;     for (int j = 0; j < 16; ++j) amax = fmaxf(fmaxf(amax, fmaxf(fabsf(v[j].x), fabsf(v[j].y))), fmaxf(fabsf(v[j].z), fabsf(v[j].w)));
;     amax = wave_max(amax); const float scale = amax > 0.f ? 127.f / amax : 0.f;
; #pragma unroll
;     for (int j = 0; j < 16; ++j) ((unsigned*)(tab + (size_t)j * PT_SLICE + (size_t)e * 256))[lane] = pack_i8x4(v[j].x * scale, v[j].y * scale, v[j].z * scale, v[j].w * scale);
	v_max_f32_e64 v91, |v35|, |v35|
	v_max_f32_e64 v92, |v34|, |v34|
	v_max_f32_e64 v93, |v37|, |v37|
	v_max_f32_e64 v94, |v36|, |v36|
	v_max_f32_e32 v81, v88, v87
	v_max_f32_e32 v82, v90, v89
	v_max3_f32 v58, v58, v67, v80
	s_waitcnt vmcnt(40)
	v_max_f32_e64 v95, |v31|, |v31|
	v_max_f32_e32 v83, v92, v91
	v_max_f32_e32 v84, v94, v93
	v_max3_f32 v58, v58, v81, v82
	v_max_f32_e64 v59, |v30|, |v30|
	v_max_f32_e64 v66, |v33|, |v33|
	v_max_f32_e64 v67, |v32|, |v32|
	v_max3_f32 v58, v58, v83, v84
	v_max_f32_e32 v59, v59, v95
	v_max_f32_e32 v66, v67, v66
	v_max3_f32 v58, v58, v59, v66
	s_waitcnt vmcnt(39)
	v_max_f32_e64 v59, |v27|, |v27|
	v_max_f32_e64 v66, |v26|, |v26|
	v_max_f32_e32 v59, v66, v59
	v_max_f32_e64 v66, |v29|, |v29|
	v_max_f32_e64 v67, |v28|, |v28|
	v_max_f32_e32 v66, v67, v66
	v_max3_f32 v58, v58, v59, v66
	s_waitcnt vmcnt(38)
	v_max_f32_e64 v59, |v23|, |v23|
	v_max_f32_e64 v66, |v22|, |v22|
	v_max_f32_e32 v59, v66, v59
	v_max_f32_e64 v66, |v25|, |v25|
	v_max_f32_e64 v67, |v24|, |v24|
	v_max_f32_e32 v66, v67, v66
	v_max3_f32 v58, v58, v59, v66
	s_waitcnt vmcnt(37)
	v_max_f32_e64 v59, |v19|, |v19|
	v_max_f32_e64 v66, |v18|, |v18|
	v_max_f32_e32 v59, v66, v59
	v_max_f32_e64 v66, |v21|, |v21|
	v_max_f32_e64 v67, |v20|, |v20|
	v_max_f32_e32 v66, v67, v66
	v_max3_f32 v58, v58, v59, v66
	s_waitcnt vmcnt(36)
	v_max_f32_e64 v59, |v15|, |v15|
	v_max_f32_e64 v66, |v14|, |v14|
	v_max_f32_e32 v59, v66, v59
	v_max_f32_e64 v66, |v17|, |v17|
	v_max_f32_e64 v67, |v16|, |v16|
	v_max_f32_e32 v66, v67, v66
	v_max3_f32 v58, v58, v59, v66
	s_waitcnt vmcnt(35)
	v_max_f32_e64 v59, |v11|, |v11|
	v_max_f32_e64 v66, |v10|, |v10|
	v_max_f32_e32 v59, v66, v59
	v_max_f32_e64 v66, |v13|, |v13|
	v_max_f32_e64 v67, |v12|, |v12|
	v_max_f32_e32 v66, v67, v66
	v_max3_f32 v58, v58, v59, v66
	s_waitcnt vmcnt(34)
	v_max_f32_e64 v59, |v7|, |v7|
	v_max_f32_e64 v66, |v6|, |v6|
	v_max_f32_e32 v59, v66, v59
	v_max_f32_e64 v66, |v9|, |v9|
	v_max_f32_e64 v67, |v8|, |v8|
	v_max_f32_e32 v66, v67, v66
	v_max3_f32 v58, v58, v59, v66
	s_waitcnt vmcnt(33)
	v_max_f32_e64 v59, |v3|, |v3|
	v_max_f32_e64 v66, |v2|, |v2|
	v_max_f32_e32 v59, v66, v59
	v_max_f32_e64 v66, |v5|, |v5|
	v_max_f32_e64 v67, |v4|, |v4|
	v_max_f32_e32 v66, v67, v66
	v_max3_f32 v58, v58, v59, v66
	ds_bpermute_b32 v59, v60, v58
	s_waitcnt lgkmcnt(0)
	v_max_f32_e32 v59, v59, v59
	v_max_f32_e32 v58, v58, v59
	ds_bpermute_b32 v59, v61, v58
	s_waitcnt lgkmcnt(0)
	v_max_f32_e32 v59, v59, v59
	v_max_f32_e32 v58, v58, v59
	ds_bpermute_b32 v59, v62, v58
	s_waitcnt lgkmcnt(0)
	v_max_f32_e32 v59, v59, v59
	v_max_f32_e32 v58, v58, v59
	ds_bpermute_b32 v59, v63, v58
	s_waitcnt lgkmcnt(0)
	v_max_f32_e32 v59, v59, v59
	v_max_f32_e32 v58, v58, v59
	ds_bpermute_b32 v59, v64, v58
	s_waitcnt lgkmcnt(0)
	v_max_f32_e32 v59, v59, v59
	v_max_f32_e32 v58, v58, v59
	ds_bpermute_b32 v59, v65, v58
	s_waitcnt lgkmcnt(0)
	v_max_f32_e32 v59, v59, v59
	v_max_f32_e32 v66, v58, v59
	v_div_scale_f32 v58, s[34:35], v66, v66, s69
	v_rcp_f32_e32 v59, v58
	s_and_b32 s34, s30, 0x3fff
	s_add_u32 s30, s33, s31
	s_addc_u32 s31, s46, 0
	v_fma_f32 v67, -v58, v59, 1.0
	v_fmac_f32_e32 v59, v67, v59
	v_div_scale_f32 v67, vcc, s69, v66, s69
	v_mul_f32_e32 v76, v67, v59
	v_fma_f32 v77, -v58, v76, v67
	v_fmac_f32_e32 v76, v77, v59
	v_fma_f32 v58, -v58, v76, v67
	v_div_fmas_f32 v58, v58, v59, v76
	v_div_fixup_f32 v58, v58, v66, s69
	v_cmp_lt_f32_e32 vcc, 0, v66
	s_lshl_b32 s35, s34, 8
	s_add_u32 s30, s30, s35
	v_cndmask_b32_e32 v67, 0, v58, vcc
	v_mul_f32_e32 v69, v69, v67
	v_mul_f32_e32 v68, v68, v67
	v_mul_f32_e32 v70, v70, v67
	v_mul_f32_e32 v71, v71, v67
	v_rndne_f32_e32 v69, v69
	v_rndne_f32_e32 v68, v68
	v_cvt_i32_f32_e32 v69, v69
	v_rndne_f32_e32 v70, v70
	v_rndne_f32_e32 v71, v71
	v_cvt_i32_f32_e32 v68, v68
	v_cvt_i32_f32_sdwa v70, v70 dst_sel:WORD_1 dst_unused:UNUSED_PAD src0_sel:DWORD
	v_cvt_i32_f32_e32 v71, v71
	v_lshlrev_b32_e32 v69, 8, v69
	v_and_b32_e32 v69, 0xff00, v69
	v_and_b32_e32 v70, 0xff0000, v70
	v_perm_b32 v68, v71, v68, s70
	s_addc_u32 s31, s31, 0
	v_or3_b32 v68, v68, v69, v70
	v_mul_f32_e32 v69, v73, v67
	global_store_dword v204, v68, s[30:31]
	v_mul_f32_e32 v68, v72, v67
	v_mul_f32_e32 v70, v74, v67
	v_mul_f32_e32 v71, v75, v67
	v_rndne_f32_e32 v69, v69
	v_rndne_f32_e32 v68, v68
	v_cvt_i32_f32_e32 v69, v69
	v_rndne_f32_e32 v70, v70
	v_rndne_f32_e32 v71, v71
	v_mul_f32_e32 v55, v55, v67
	v_cvt_i32_f32_e32 v68, v68
	v_cvt_i32_f32_sdwa v70, v70 dst_sel:WORD_1 dst_unused:UNUSED_PAD src0_sel:DWORD
	v_cvt_i32_f32_e32 v71, v71
	v_mul_f32_e32 v54, v54, v67
	v_mul_f32_e32 v56, v56, v67
	v_mul_f32_e32 v57, v57, v67
	v_rndne_f32_e32 v55, v55
	v_rndne_f32_e32 v54, v54
	v_cvt_i32_f32_e32 v55, v55
	v_rndne_f32_e32 v56, v56
	v_rndne_f32_e32 v57, v57
	v_mul_f32_e32 v51, v51, v67
	v_cvt_i32_f32_e32 v54, v54
	v_cvt_i32_f32_sdwa v56, v56 dst_sel:WORD_1 dst_unused:UNUSED_PAD src0_sel:DWORD
	v_cvt_i32_f32_e32 v57, v57
	v_mul_f32_e32 v50, v50, v67
	v_mul_f32_e32 v52, v52, v67
	v_mul_f32_e32 v53, v53, v67
	v_rndne_f32_e32 v51, v51
	v_lshlrev_b32_e32 v69, 8, v69
	v_rndne_f32_e32 v50, v50
	v_cvt_i32_f32_e32 v51, v51
	v_rndne_f32_e32 v52, v52
	v_rndne_f32_e32 v53, v53
	v_mul_f32_e32 v47, v47, v67
	v_lshl_add_u64 v[58:59], s[30:31], 0, v[204:205]
	v_and_b32_e32 v69, 0xff00, v69
	v_and_b32_e32 v70, 0xff0000, v70
	v_perm_b32 v68, v71, v68, s70
	s_mov_b32 s30, 0x400000
	v_cvt_i32_f32_e32 v50, v50
	v_cvt_i32_f32_sdwa v52, v52 dst_sel:WORD_1 dst_unused:UNUSED_PAD src0_sel:DWORD
	v_cvt_i32_f32_e32 v53, v53
	v_mul_f32_e32 v46, v46, v67
	v_mul_f32_e32 v48, v48, v67
	v_mul_f32_e32 v49, v49, v67
	v_rndne_f32_e32 v47, v47
	v_or3_b32 v70, v68, v69, v70
	v_add_co_u32_e32 v68, vcc, s30, v58
; __device__ __forceinline__ void pt_proc(unsigned char* PT, const f32x4* v, int r, int lane) {
;     ...
;     amax = wave_max(amax); const float scale = amax > 0.f ? 127.f / amax : 0.f;
; #pragma unroll
;     for (int j = 0; j < 16; ++j) ((unsigned*)(tab + (size_t)j * PT_SLICE + (size_t)e * 256))[lane] = pack_i8x4(v[j].x * scale, v[j].y * scale, v[j].z * scale, v[j].w * scale);
	v_lshlrev_b32_e32 v55, 8, v55
	v_rndne_f32_e32 v46, v46
	v_cvt_i32_f32_e32 v47, v47
	v_rndne_f32_e32 v48, v48
	v_rndne_f32_e32 v49, v49
	v_mul_f32_e32 v43, v43, v67
	v_addc_co_u32_e32 v69, vcc, 0, v59, vcc
	v_and_b32_e32 v55, 0xff00, v55
	v_and_b32_e32 v56, 0xff0000, v56
	v_perm_b32 v54, v57, v54, s70
	s_mov_b32 s30, 0x800000
	v_cvt_i32_f32_e32 v46, v46
	v_cvt_i32_f32_sdwa v48, v48 dst_sel:WORD_1 dst_unused:UNUSED_PAD src0_sel:DWORD
	v_cvt_i32_f32_e32 v49, v49
	v_mul_f32_e32 v42, v42, v67
	v_mul_f32_e32 v44, v44, v67
	v_mul_f32_e32 v45, v45, v67
	v_rndne_f32_e32 v43, v43
	v_or3_b32 v56, v54, v55, v56
	v_add_co_u32_e32 v54, vcc, s30, v58
	v_lshlrev_b32_e32 v51, 8, v51
	v_rndne_f32_e32 v42, v42
	v_cvt_i32_f32_e32 v43, v43
	v_rndne_f32_e32 v44, v44
	v_rndne_f32_e32 v45, v45
	v_mul_f32_e32 v39, v39, v67
	v_addc_co_u32_e32 v55, vcc, 0, v59, vcc
	v_and_b32_e32 v51, 0xff00, v51
	v_and_b32_e32 v52, 0xff0000, v52
	v_perm_b32 v50, v53, v50, s70
	s_mov_b32 s30, 0xc00000
	v_cvt_i32_f32_e32 v42, v42
	v_cvt_i32_f32_sdwa v44, v44 dst_sel:WORD_1 dst_unused:UNUSED_PAD src0_sel:DWORD
	v_cvt_i32_f32_e32 v45, v45
	v_mul_f32_e32 v38, v38, v67
	v_mul_f32_e32 v40, v40, v67
	v_mul_f32_e32 v41, v41, v67
	v_rndne_f32_e32 v39, v39
	v_or3_b32 v52, v50, v51, v52
	v_add_co_u32_e32 v50, vcc, s30, v58
	v_lshlrev_b32_e32 v47, 8, v47
	v_rndne_f32_e32 v38, v38
	v_cvt_i32_f32_e32 v39, v39
	v_rndne_f32_e32 v40, v40
	v_rndne_f32_e32 v41, v41
	v_mul_f32_e32 v35, v35, v67
	v_addc_co_u32_e32 v51, vcc, 0, v59, vcc
	v_and_b32_e32 v47, 0xff00, v47
	v_and_b32_e32 v48, 0xff0000, v48
	v_perm_b32 v46, v49, v46, s70
	s_mov_b32 s30, 0x1000000
	v_cvt_i32_f32_e32 v38, v38
	v_cvt_i32_f32_sdwa v40, v40 dst_sel:WORD_1 dst_unused:UNUSED_PAD src0_sel:DWORD
	v_cvt_i32_f32_e32 v41, v41
	v_mul_f32_e32 v34, v34, v67
	v_mul_f32_e32 v36, v36, v67
	v_mul_f32_e32 v37, v37, v67
	v_rndne_f32_e32 v35, v35
	v_or3_b32 v48, v46, v47, v48
	v_add_co_u32_e32 v46, vcc, s30, v58
	v_lshlrev_b32_e32 v43, 8, v43
	v_rndne_f32_e32 v34, v34
	v_cvt_i32_f32_e32 v35, v35
	v_rndne_f32_e32 v36, v36
	v_rndne_f32_e32 v37, v37
	v_mul_f32_e32 v31, v31, v67
	v_addc_co_u32_e32 v47, vcc, 0, v59, vcc
	v_and_b32_e32 v43, 0xff00, v43
	v_and_b32_e32 v44, 0xff0000, v44
	v_perm_b32 v42, v45, v42, s70
	s_mov_b32 s30, 0x1400000
	v_cvt_i32_f32_e32 v34, v34
	v_cvt_i32_f32_sdwa v36, v36 dst_sel:WORD_1 dst_unused:UNUSED_PAD src0_sel:DWORD
	v_cvt_i32_f32_e32 v37, v37
	v_mul_f32_e32 v30, v30, v67
	v_mul_f32_e32 v32, v32, v67
	v_mul_f32_e32 v33, v33, v67
	v_rndne_f32_e32 v31, v31
	v_or3_b32 v44, v42, v43, v44
	v_add_co_u32_e32 v42, vcc, s30, v58
	v_lshlrev_b32_e32 v39, 8, v39
	v_rndne_f32_e32 v30, v30
	v_cvt_i32_f32_e32 v31, v31
	v_rndne_f32_e32 v32, v32
	v_rndne_f32_e32 v33, v33
	v_mul_f32_e32 v27, v27, v67
	v_addc_co_u32_e32 v43, vcc, 0, v59, vcc
	v_and_b32_e32 v39, 0xff00, v39
	v_and_b32_e32 v40, 0xff0000, v40
	v_perm_b32 v38, v41, v38, s70
	s_mov_b32 s30, 0x1800000
	v_cvt_i32_f32_e32 v30, v30
	v_cvt_i32_f32_sdwa v32, v32 dst_sel:WORD_1 dst_unused:UNUSED_PAD src0_sel:DWORD
	v_cvt_i32_f32_e32 v33, v33
	v_mul_f32_e32 v26, v26, v67
	v_mul_f32_e32 v28, v28, v67
	v_mul_f32_e32 v29, v29, v67
	v_rndne_f32_e32 v27, v27
	v_or3_b32 v40, v38, v39, v40
	v_add_co_u32_e32 v38, vcc, s30, v58
	v_lshlrev_b32_e32 v35, 8, v35
	v_rndne_f32_e32 v26, v26
	v_cvt_i32_f32_e32 v27, v27
	v_rndne_f32_e32 v28, v28
	v_rndne_f32_e32 v29, v29
	v_mul_f32_e32 v23, v23, v67
	v_addc_co_u32_e32 v39, vcc, 0, v59, vcc
	v_and_b32_e32 v35, 0xff00, v35
	v_and_b32_e32 v36, 0xff0000, v36
	v_perm_b32 v34, v37, v34, s70
	s_mov_b32 s30, 0x1c00000
	v_cvt_i32_f32_e32 v26, v26
	v_cvt_i32_f32_sdwa v28, v28 dst_sel:WORD_1 dst_unused:UNUSED_PAD src0_sel:DWORD
	v_cvt_i32_f32_e32 v29, v29
	v_mul_f32_e32 v22, v22, v67
	v_mul_f32_e32 v24, v24, v67
	v_mul_f32_e32 v25, v25, v67
	v_rndne_f32_e32 v23, v23
	v_or3_b32 v36, v34, v35, v36
	v_add_co_u32_e32 v34, vcc, s30, v58
	v_lshlrev_b32_e32 v31, 8, v31
	v_rndne_f32_e32 v22, v22
	v_cvt_i32_f32_e32 v23, v23
	v_rndne_f32_e32 v24, v24
	v_rndne_f32_e32 v25, v25
	v_mul_f32_e32 v19, v19, v67
	v_addc_co_u32_e32 v35, vcc, 0, v59, vcc
	v_and_b32_e32 v31, 0xff00, v31
	v_and_b32_e32 v32, 0xff0000, v32
	v_perm_b32 v30, v33, v30, s70
	s_brev_b32 s30, 64
	v_cvt_i32_f32_e32 v22, v22
	v_cvt_i32_f32_sdwa v24, v24 dst_sel:WORD_1 dst_unused:UNUSED_PAD src0_sel:DWORD
	v_cvt_i32_f32_e32 v25, v25
	v_mul_f32_e32 v18, v18, v67
	v_mul_f32_e32 v20, v20, v67
	v_mul_f32_e32 v21, v21, v67
	v_rndne_f32_e32 v19, v19
	v_or3_b32 v32, v30, v31, v32
	v_add_co_u32_e32 v30, vcc, s30, v58
	v_lshlrev_b32_e32 v27, 8, v27
	v_rndne_f32_e32 v18, v18
	v_cvt_i32_f32_e32 v19, v19
	v_rndne_f32_e32 v20, v20
	v_rndne_f32_e32 v21, v21
	v_mul_f32_e32 v15, v15, v67
	v_addc_co_u32_e32 v31, vcc, 0, v59, vcc
	v_and_b32_e32 v27, 0xff00, v27
	v_and_b32_e32 v28, 0xff0000, v28
	v_perm_b32 v26, v29, v26, s70
	s_mov_b32 s30, 0x2400000
	v_cvt_i32_f32_e32 v18, v18
	v_cvt_i32_f32_sdwa v20, v20 dst_sel:WORD_1 dst_unused:UNUSED_PAD src0_sel:DWORD
	v_cvt_i32_f32_e32 v21, v21
	v_mul_f32_e32 v14, v14, v67
	v_mul_f32_e32 v16, v16, v67
	v_mul_f32_e32 v17, v17, v67
	v_rndne_f32_e32 v15, v15
	v_or3_b32 v28, v26, v27, v28
	v_add_co_u32_e32 v26, vcc, s30, v58
	v_lshlrev_b32_e32 v23, 8, v23
	v_rndne_f32_e32 v14, v14
	v_cvt_i32_f32_e32 v15, v15
	v_rndne_f32_e32 v16, v16
	v_rndne_f32_e32 v17, v17
	v_mul_f32_e32 v11, v11, v67
	v_addc_co_u32_e32 v27, vcc, 0, v59, vcc
; __device__ __forceinline__ void pt_proc(unsigned char* PT, const f32x4* v, int r, int lane) {
;     ...
;     amax = wave_max(amax); const float scale = amax > 0.f ? 127.f / amax : 0.f;
; #pragma unroll
;     for (int j = 0; j < 16; ++j) ((unsigned*)(tab + (size_t)j * PT_SLICE + (size_t)e * 256))[lane] = pack_i8x4(v[j].x * scale, v[j].y * scale, v[j].z * scale, v[j].w * scale);
;     if (lane == 0) ((float*)(PT + (tb ? PT_VS : PT_US)))[e] = amax * (1.f / 127.f);
	v_and_b32_e32 v23, 0xff00, v23
	v_and_b32_e32 v24, 0xff0000, v24
	v_perm_b32 v22, v25, v22, s70
	s_mov_b32 s30, 0x2800000
	v_cvt_i32_f32_e32 v14, v14
	v_cvt_i32_f32_sdwa v16, v16 dst_sel:WORD_1 dst_unused:UNUSED_PAD src0_sel:DWORD
	v_cvt_i32_f32_e32 v17, v17
	v_mul_f32_e32 v10, v10, v67
	v_mul_f32_e32 v12, v12, v67
	v_mul_f32_e32 v13, v13, v67
	v_rndne_f32_e32 v11, v11
	v_or3_b32 v24, v22, v23, v24
	v_add_co_u32_e32 v22, vcc, s30, v58
	v_lshlrev_b32_e32 v19, 8, v19
	v_rndne_f32_e32 v10, v10
	v_cvt_i32_f32_e32 v11, v11
	v_rndne_f32_e32 v12, v12
	v_rndne_f32_e32 v13, v13
	v_mul_f32_e32 v7, v7, v67
	v_addc_co_u32_e32 v23, vcc, 0, v59, vcc
	v_and_b32_e32 v19, 0xff00, v19
	v_and_b32_e32 v20, 0xff0000, v20
	v_perm_b32 v18, v21, v18, s70
	v_cvt_i32_f32_e32 v10, v10
	v_cvt_i32_f32_sdwa v12, v12 dst_sel:WORD_1 dst_unused:UNUSED_PAD src0_sel:DWORD
	v_cvt_i32_f32_e32 v13, v13
	v_mul_f32_e32 v6, v6, v67
	v_mul_f32_e32 v8, v8, v67
	v_mul_f32_e32 v9, v9, v67
	v_rndne_f32_e32 v7, v7
	v_or3_b32 v20, v18, v19, v20
	v_add_co_u32_e32 v18, vcc, s71, v58
	v_lshlrev_b32_e32 v15, 8, v15
	v_rndne_f32_e32 v6, v6
	v_cvt_i32_f32_e32 v7, v7
	v_rndne_f32_e32 v8, v8
	v_rndne_f32_e32 v9, v9
	v_mul_f32_e32 v3, v3, v67
	v_addc_co_u32_e32 v19, vcc, 0, v59, vcc
	v_and_b32_e32 v15, 0xff00, v15
	v_and_b32_e32 v16, 0xff0000, v16
	v_perm_b32 v14, v17, v14, s70
	v_cvt_i32_f32_e32 v6, v6
	v_cvt_i32_f32_sdwa v8, v8 dst_sel:WORD_1 dst_unused:UNUSED_PAD src0_sel:DWORD
	v_cvt_i32_f32_e32 v9, v9
	v_mul_f32_e32 v2, v2, v67
	v_mul_f32_e32 v4, v4, v67
	v_mul_f32_e32 v5, v5, v67
	v_rndne_f32_e32 v3, v3
	v_or3_b32 v16, v14, v15, v16
	v_add_co_u32_e32 v14, vcc, s72, v58
	v_lshlrev_b32_e32 v11, 8, v11
	v_rndne_f32_e32 v2, v2
	v_cvt_i32_f32_e32 v3, v3
	v_rndne_f32_e32 v4, v4
	v_rndne_f32_e32 v5, v5
	v_addc_co_u32_e32 v15, vcc, 0, v59, vcc
	v_and_b32_e32 v11, 0xff00, v11
	v_and_b32_e32 v12, 0xff0000, v12
	v_perm_b32 v10, v13, v10, s70
	v_cvt_i32_f32_e32 v2, v2
	v_cvt_i32_f32_sdwa v4, v4 dst_sel:WORD_1 dst_unused:UNUSED_PAD src0_sel:DWORD
	v_cvt_i32_f32_e32 v5, v5
	v_or3_b32 v12, v10, v11, v12
	v_add_co_u32_e32 v10, vcc, s73, v58
	v_lshlrev_b32_e32 v7, 8, v7
	s_nop 0
	v_addc_co_u32_e32 v11, vcc, 0, v59, vcc
	v_and_b32_e32 v7, 0xff00, v7
	v_and_b32_e32 v8, 0xff0000, v8
	v_perm_b32 v6, v9, v6, s70
	v_or3_b32 v8, v6, v7, v8
	v_add_co_u32_e32 v6, vcc, s74, v58
	v_lshlrev_b32_e32 v3, 8, v3
	s_nop 0
	v_addc_co_u32_e32 v7, vcc, 0, v59, vcc
	v_and_b32_e32 v3, 0xff00, v3
	v_and_b32_e32 v4, 0xff0000, v4
	v_perm_b32 v2, v5, v2, s70
	v_or3_b32 v4, v2, v3, v4
	v_add_co_u32_e32 v2, vcc, 0x3c00000, v58
	global_store_dword v[68:69], v70, off
	s_nop 0
	v_addc_co_u32_e32 v3, vcc, 0, v59, vcc
	global_store_dword v[54:55], v56, off
	global_store_dword v[50:51], v52, off
	global_store_dword v[46:47], v48, off
	global_store_dword v[42:43], v44, off
	global_store_dword v[38:39], v40, off
	global_store_dword v[34:35], v36, off
	global_store_dword v[30:31], v32, off
	global_store_dword v[26:27], v28, off
	global_store_dword v[22:23], v24, off
	global_store_dword v[18:19], v20, off
	global_store_dword v[14:15], v16, off
	global_store_dword v[10:11], v12, off
	global_store_dword v[6:7], v8, off
	global_store_dword v[2:3], v4, off
	s_and_saveexec_b64 s[30:31], s[6:7]
	s_cbranch_execz .Lside_jA
	s_and_b64 s[10:11], s[10:11], exec
	s_cselect_b32 s10, s75, 0x8010000
	s_add_u32 s10, s33, s10
	s_addc_u32 s11, s46, 0
	s_lshl_b32 s34, s34, 2
	v_mul_f32_e32 v2, 0x3c010204, v66
	v_mov_b32_e32 v3, s34
	global_store_dword v3, v2, s[10:11]
	s_branch .Lside_jA
.Lside_jA:
	s_or_b64 exec, exec, s[30:31]
	s_add_i32 s23, s23, 8
	s_add_i32 s25, s25, 0x8000
	s_cmp_eq_u32 s23, 64
	s_cbranch_scc1 .Lside_last
	s_and_b32 s10, s25, 0x3fff000
	s_add_i32 s30, s66, s23
	s_lshl_b32 s36, s10, 2
	s_cmpk_lt_u32 s30, 0x4000
	s_cselect_b64 s[10:11], -1, 0
	s_and_b64 s[34:35], s[10:11], exec
	s_cselect_b32 s34, s12, s14
	s_cselect_b32 s35, s13, s15
	s_cselect_b32 s31, 0, 0x4000000
	s_add_u32 s34, s34, s36
	s_addc_u32 s35, s35, 0
	v_lshlrev_b32_e32 v204, 4, v194
	s_movk_i32 s36, 0x2000
	v_lshl_add_u64 v[2:3], s[34:35], 0, v[204:205]
	v_add_co_u32_e32 v4, vcc, s36, v2
	global_load_dwordx4 v[68:71], v204, s[34:35] nt
	global_load_dwordx4 v[72:75], v204, s[34:35] offset:1024 nt
	global_load_dwordx4 v[54:57], v204, s[34:35] offset:2048 nt
	global_load_dwordx4 v[50:53], v204, s[34:35] offset:3072 nt
	v_addc_co_u32_e32 v5, vcc, 0, v3, vcc
	global_load_dwordx4 v[46:49], v[4:5], off offset:-4096 nt
	s_movk_i32 s37, 0x1000
	v_add_co_u32_e32 v6, vcc, s37, v2
	s_movk_i32 s34, 0x3000
	s_nop 0
	v_addc_co_u32_e32 v7, vcc, 0, v3, vcc
	global_load_dwordx4 v[42:45], v[6:7], off offset:1024 nt
	global_load_dwordx4 v[38:41], v[6:7], off offset:2048 nt
	global_load_dwordx4 v[34:37], v[6:7], off offset:3072 nt
	global_load_dwordx4 v[30:33], v[4:5], off nt
	global_load_dwordx4 v[26:29], v[4:5], off offset:1024 nt
	global_load_dwordx4 v[22:25], v[4:5], off offset:2048 nt
	v_add_co_u32_e32 v2, vcc, s34, v2
	v_lshlrev_b32_e32 v204, 2, v194
	s_nop 0
	v_addc_co_u32_e32 v3, vcc, 0, v3, vcc
	global_load_dwordx4 v[18:21], v[4:5], off offset:3072 nt
	global_load_dwordx4 v[14:17], v[2:3], off nt
	global_load_dwordx4 v[10:13], v[2:3], off offset:1024 nt
	global_load_dwordx4 v[6:9], v[2:3], off offset:2048 nt
	s_nop 0
	global_load_dwordx4 v[2:5], v[2:3], off offset:3072 nt
	s_branch .Lside_pB

; __device__ __forceinline__ void phase_peer_tables(const Frame& F, const Args& a, int r_lo, int r_hi, int gw, int NGW) {
;     unsigned char* PT = a.ws + WS_PT; const int lane = F.lane;
;     int r = r_lo + gw; if (r >= r_hi) return;
;     f32x4 vA[16], vB[16];
;     pt_load(a.in[17], a.in[18], vA, r, lane);
; __global__ void __launch_bounds__(NTHREADS, 2) fwd(Args args) {
;     ...
;         { const int nwg = (T / 256) * (ZW / 256), rem = nwg % F.G;
;           if (rem != 0 && F.vid >= rem) phase_peer_tables(F, args, side_rows, side_rows + PT_EARLY_ROWS, (F.vid - rem) * NWAVES + F.wave, (F.G - rem) * NWAVES);
;           else if (rem == 0) phase_peer_tables(F, args, side_rows, side_rows + PT_EARLY_ROWS, F.bid * NWAVES + F.wave, F.G * NWAVES); }
.LBB0_208:
	s_and_b64 s[0:1], s[0:1], exec
	s_cselect_b32 s10, 0x4000, 0
	s_abs_i32 s0, s96
	v_cvt_f32_u32_e32 v1, s0
	s_sub_i32 s1, 0, s0
	s_or_b32 s8, s10, 0x3000
	s_lshl_b32 s9, s96, 3
	v_rcp_iflag_f32_e32 v1, v1
	s_nop 0
	v_mul_f32_e32 v1, 0x4f7ffffe, v1
	v_cvt_u32_f32_e32 v1, v1
	s_nop 0
	v_readfirstlane_b32 s2, v1
	s_mul_i32 s1, s1, s2
	s_mul_hi_u32 s1, s2, s1
	s_add_i32 s2, s2, s1
	s_mul_hi_u32 s1, s2, 0x7a0
	s_mul_i32 s1, s1, s0
	s_sub_i32 s1, 0x7a0, s1
	s_sub_i32 s2, s1, s0
	s_cmp_ge_u32 s1, s0
	s_cselect_b32 s1, s2, s1
	s_sub_i32 s2, s1, s0
	s_cmp_ge_u32 s1, s0
	s_cselect_b32 s0, s2, s1
	s_cmp_eq_u32 s0, 0
	s_cbranch_scc1 .LBB0_224
	s_cmp_lt_i32 s84, s0
	s_cbranch_scc1 .LBB0_223
	s_sub_i32 s1, s84, s0
	s_lshl_b32 s1, s1, 3
	v_readlane_b32 s2, v245, 7
	s_add_i32 s1, s1, s2
	s_cmpk_gt_u32 s1, 0x2fff
	s_cbranch_scc1 .LBB0_223
	s_or_b32 s2, s1, s10
	s_cmpk_lt_u32 s2, 0x4000
	s_cselect_b32 s4, s13, s15
	s_cselect_b32 s5, s12, s14
	s_lshl_b32 s2, s1, 12
	s_mov_b32 s3, 0
	s_lshl_b64 s[2:3], s[2:3], 2
	s_add_u32 s2, s5, s2
	v_mov_b32_e32 v133, 0
	s_addc_u32 s3, s4, s3
	v_lshlrev_b32_e32 v130, 4, v194
	v_mov_b32_e32 v131, v133
	v_lshl_add_u64 v[26:27], s[2:3], 0, v[130:131]
	s_movk_i32 s11, 0x1000
	v_add_co_u32_e32 v66, vcc, s11, v26
	s_movk_i32 s1, 0x2000
	s_nop 0
	v_addc_co_u32_e32 v67, vcc, 0, v27, vcc
	v_add_co_u32_e32 v28, vcc, s1, v26
	global_load_dwordx4 v[2:5], v130, s[2:3] offset:1024 nt
	global_load_dwordx4 v[6:9], v130, s[2:3] offset:2048 nt
	v_addc_co_u32_e32 v29, vcc, 0, v27, vcc
	global_load_dwordx4 v[10:13], v130, s[2:3] offset:3072 nt
	global_load_dwordx4 v[14:17], v[28:29], off offset:-4096 nt
	global_load_dwordx4 v[18:21], v[66:67], off offset:1024 nt
	global_load_dwordx4 v[22:25], v[66:67], off offset:2048 nt
	global_load_dwordx4 v[30:33], v[28:29], off nt
	global_load_dwordx4 v[34:37], v[28:29], off offset:1024 nt
	global_load_dwordx4 v[42:45], v[28:29], off offset:2048 nt
	global_load_dwordx4 v[46:49], v[28:29], off offset:3072 nt
	s_movk_i32 s1, 0x3000
	v_add_co_u32_e32 v68, vcc, s1, v26
	v_mbcnt_lo_u32_b32 v1, -1, 0
	s_nop 0
	v_addc_co_u32_e32 v69, vcc, 0, v27, vcc
	global_load_dwordx4 v[38:41], v[66:67], off offset:3072 nt
	global_load_dwordx4 v[50:53], v[68:69], off nt
	global_load_dwordx4 v[54:57], v[68:69], off offset:1024 nt
	global_load_dwordx4 v[58:61], v[68:69], off offset:2048 nt
	global_load_dwordx4 v[26:29], v130, s[2:3] nt
	global_load_dwordx4 v[62:65], v[68:69], off offset:3072 nt
	v_mbcnt_hi_u32_b32 v66, -1, v1
	v_and_b32_e32 v1, 64, v66
	v_add_u32_e32 v67, 64, v1
	v_xor_b32_e32 v1, 1, v66
	v_cmp_lt_i32_e32 vcc, v1, v67
	v_xor_b32_e32 v68, 2, v66
	v_readlane_b32 s21, v245, 7
	v_cndmask_b32_e32 v1, v66, v1, vcc
	v_cmp_lt_i32_e32 vcc, v68, v67
	s_add_i32 s1, s10, s21
	s_lshl_b32 s2, s0, 3
	v_cndmask_b32_e32 v68, v66, v68, vcc
	v_lshlrev_b32_e32 v136, 2, v68
	v_xor_b32_e32 v68, 4, v66
	v_cmp_lt_i32_e32 vcc, v68, v67
	s_sub_i32 s17, s1, s2
	s_lshl_b32 s2, s96, 4
	v_cndmask_b32_e32 v68, v66, v68, vcc
	v_lshlrev_b32_e32 v137, 2, v68
	v_xor_b32_e32 v68, 8, v66
	v_cmp_lt_i32_e32 vcc, v68, v67
	s_lshl_b32 s3, s0, 4
	s_sub_i32 s18, s2, s3
	v_cndmask_b32_e32 v68, v66, v68, vcc
	v_lshlrev_b32_e32 v138, 2, v68
	v_xor_b32_e32 v68, 16, v66
	v_cmp_lt_i32_e32 vcc, v68, v67
	s_add_i32 s2, s1, s2
	s_mul_i32 s4, s0, 24
	v_cndmask_b32_e32 v68, v66, v68, vcc
	v_lshlrev_b32_e32 v139, 2, v68
	v_xor_b32_e32 v68, 32, v66
	s_sub_i32 s19, s2, s4
	s_lshl_b32 s2, s96, 16
	s_mul_i32 s4, s0, 0x18000
	v_cmp_lt_i32_e32 vcc, v68, v67
	s_sub_i32 s20, s2, s4
	s_lshl_b32 s4, s84, 15
	s_lshl_b32 s5, s10, 12
	s_add_i32 s1, s1, s9
	v_cndmask_b32_e32 v66, v66, v68, vcc
	s_add_i32 s4, s4, s5
	s_lshl_b32 s5, s21, 12
	s_lshl_b32 s0, s0, 16
	s_sub_i32 s23, s1, s3
	s_lshl_b32 s1, s96, 15
	v_lshlrev_b32_e32 v1, 2, v1
	v_lshlrev_b32_e32 v140, 2, v66
	s_lshl_b32 s16, s84, 3
	s_add_i32 s21, s4, s5
	s_sub_i32 s22, s2, s0
	s_sub_i32 s24, s1, s0
	s_mov_b32 s25, 0x42fe0000
	s_mov_b32 s26, 0x40c0c00
	s_mov_b32 s27, 0x400000
	s_mov_b32 s28, 0x800000
	s_mov_b32 s29, 0xc00000
	s_mov_b32 s30, 0x1000000
	s_mov_b32 s31, 0x1400000
	s_mov_b32 s34, 0x1800000
	s_mov_b32 s35, 0x1c00000
	s_brev_b32 s36, 64
	s_mov_b32 s37, 0x2400000
	s_mov_b32 s38, 0x2800000
	s_mov_b32 s39, 0x2c00000
	s_mov_b32 s40, 0x3000000
	s_mov_b32 s41, 0x3400000
	s_mov_b32 s42, 0x3800000
	s_brev_b32 s43, 16
	s_branch .LBB0_214

; __device__ __forceinline__ void pt_load(const float* tu, const float* tv, f32x4* v, int r, int lane) {
;     const f32x4* sp = (const f32x4*)(((r >> 14) ? tv : tu) + (size_t)(r & 16383) * D) + lane;
; #pragma unroll
;     for (int j = 0; j < 16; ++j) v[j] = sp[64 * j];
; }
; __device__ __forceinline__ void phase_peer_tables(const Frame& F, const Args& a, int r_lo, int r_hi, int gw, int NGW) {
;     ...
;         const int r1 = r + NGW; const bool h1 = r1 < r_hi;
;         if (h1) pt_load(a.in[17], a.in[18], vB, r1, lane);
.LBB0_214:
	s_add_i32 s44, s16, s23
	s_cmp_lt_i32 s44, s8
	s_cselect_b64 s[0:1], -1, 0
	s_cmp_ge_i32 s44, s8
	s_cbranch_scc1 .LBB0_216
	s_cmpk_lt_u32 s44, 0x4000
	s_cselect_b32 s3, s13, s15
	s_cselect_b32 s2, s12, s14
	s_add_i32 s4, s24, s21
	s_and_b32 s4, s4, 0x3fff000
	s_lshl_b32 s4, s4, 2
	s_add_u32 s2, s2, s4
	s_addc_u32 s3, s3, 0
	v_mov_b32_e32 v131, v133
	v_lshl_add_u64 v[114:115], s[2:3], 0, v[130:131]
	v_add_co_u32_e32 v82, vcc, s11, v114
	global_load_dwordx4 v[78:81], v130, s[2:3] nt
	global_load_dwordx4 v[74:77], v130, s[2:3] offset:1024 nt
	global_load_dwordx4 v[70:73], v130, s[2:3] offset:2048 nt
	global_load_dwordx4 v[66:69], v130, s[2:3] offset:3072 nt
	v_addc_co_u32_e32 v83, vcc, 0, v115, vcc
	v_add_co_u32_e32 v98, vcc, 0x2000, v114
	global_load_dwordx4 v[94:97], v[82:83], off nt
	global_load_dwordx4 v[90:93], v[82:83], off offset:1024 nt
	global_load_dwordx4 v[86:89], v[82:83], off offset:2048 nt
	s_nop 0
	global_load_dwordx4 v[82:85], v[82:83], off offset:3072 nt
	v_addc_co_u32_e32 v99, vcc, 0, v115, vcc
	v_add_co_u32_e32 v114, vcc, 0x3000, v114
	global_load_dwordx4 v[110:113], v[98:99], off nt
	global_load_dwordx4 v[106:109], v[98:99], off offset:1024 nt
	global_load_dwordx4 v[102:105], v[98:99], off offset:2048 nt
	s_nop 0
	global_load_dwordx4 v[98:101], v[98:99], off offset:3072 nt
	v_addc_co_u32_e32 v115, vcc, 0, v115, vcc
	global_load_dwordx4 v[126:129], v[114:115], off nt
	global_load_dwordx4 v[122:125], v[114:115], off offset:1024 nt
	global_load_dwordx4 v[118:121], v[114:115], off offset:2048 nt
	s_nop 0
	global_load_dwordx4 v[114:117], v[114:115], off offset:3072 nt

; __device__ __forceinline__ void pt_load(const float* tu, const float* tv, f32x4* v, int r, int lane) {
;     const f32x4* sp = (const f32x4*)(((r >> 14) ? tv : tu) + (size_t)(r & 16383) * D) + lane;
; #pragma unroll
;     for (int j = 0; j < 16; ++j) v[j] = sp[64 * j];
; }
; __device__ __forceinline__ void phase_peer_tables(const Frame& F, const Args& a, int r_lo, int r_hi, int gw, int NGW) {
;     ...
;         const int r2 = r1 + NGW; const bool h2 = r2 < r_hi;
;         if (h2) pt_load(a.in[17], a.in[18], vA, r2, lane);
.LBB0_219:
	s_add_i32 s0, s16, s19
	s_cmp_ge_i32 s0, s8
	s_cbranch_scc1 .LBB0_221
	s_cmpk_lt_u32 s0, 0x4000
	s_cselect_b32 s1, s13, s15
	s_cselect_b32 s0, s12, s14
	s_add_i32 s2, s20, s21
	s_and_b32 s2, s2, 0x3fff000
	s_lshl_b32 s2, s2, 2
	s_add_u32 s0, s0, s2
	s_addc_u32 s1, s1, 0
	v_mov_b32_e32 v131, v133
	v_lshl_add_u64 v[50:51], s[0:1], 0, v[130:131]
	v_add_co_u32_e32 v30, vcc, s11, v50
	global_load_dwordx4 v[26:29], v130, s[0:1] nt
	global_load_dwordx4 v[2:5], v130, s[0:1] offset:1024 nt
	global_load_dwordx4 v[6:9], v130, s[0:1] offset:2048 nt
	global_load_dwordx4 v[10:13], v130, s[0:1] offset:3072 nt
	v_addc_co_u32_e32 v31, vcc, 0, v51, vcc
	v_add_co_u32_e32 v46, vcc, 0x2000, v50
	global_load_dwordx4 v[14:17], v[30:31], off nt
	global_load_dwordx4 v[18:21], v[30:31], off offset:1024 nt
	global_load_dwordx4 v[22:25], v[30:31], off offset:2048 nt
	global_load_dwordx4 v[38:41], v[30:31], off offset:3072 nt
	v_addc_co_u32_e32 v47, vcc, 0, v51, vcc
	v_add_co_u32_e32 v62, vcc, 0x3000, v50
	global_load_dwordx4 v[30:33], v[46:47], off nt
	global_load_dwordx4 v[34:37], v[46:47], off offset:1024 nt
	global_load_dwordx4 v[42:45], v[46:47], off offset:2048 nt
	s_nop 0
	global_load_dwordx4 v[46:49], v[46:47], off offset:3072 nt
	v_addc_co_u32_e32 v63, vcc, 0, v51, vcc
	global_load_dwordx4 v[50:53], v[62:63], off nt
	global_load_dwordx4 v[54:57], v[62:63], off offset:1024 nt
	global_load_dwordx4 v[58:61], v[62:63], off offset:2048 nt
	s_nop 0
	global_load_dwordx4 v[62:65], v[62:63], off offset:3072 nt

; __device__ __forceinline__ void phase_peer_tables(const Frame& F, const Args& a, int r_lo, int r_hi, int gw, int NGW) {
;     unsigned char* PT = a.ws + WS_PT; const int lane = F.lane;
;     int r = r_lo + gw; if (r >= r_hi) return;
;     f32x4 vA[16], vB[16];
;     pt_load(a.in[17], a.in[18], vA, r, lane);
; __global__ void __launch_bounds__(NTHREADS, 2) fwd(Args args) {
;     ...
;           else if (rem == 0) phase_peer_tables(F, args, side_rows, side_rows + PT_EARLY_ROWS, F.bid * NWAVES + F.wave, F.G * NWAVES); }
.LBB0_224:
.LBB0_225:
	s_lshl_b32 s0, s94, 3
	v_readlane_b32 s1, v245, 7
	s_add_i32 s0, s1, s0
	s_cmpk_gt_i32 s0, 0x2fff
	s_cbranch_scc1 .LBB0_238
	s_add_i32 s39, s10, s0
	s_cmpk_lt_u32 s39, 0x4000
	s_cselect_b32 s1, s13, s15
	s_cselect_b32 s2, s12, s14
	s_lshl_b32 s0, s0, 14
	s_and_b32 s0, s0, 0xfffc000
	s_add_u32 s0, s2, s0
	v_mov_b32_e32 v133, 0
	s_addc_u32 s1, s1, 0
	v_lshlrev_b32_e32 v130, 4, v194
	v_mov_b32_e32 v131, v133
	s_waitcnt vmcnt(31)
	v_lshl_add_u64 v[26:27], s[0:1], 0, v[130:131]
	s_movk_i32 s11, 0x1000
	v_add_co_u32_e32 v66, vcc, s11, v26
	s_movk_i32 s2, 0x2000
	s_nop 0
	v_addc_co_u32_e32 v67, vcc, 0, v27, vcc
	v_add_co_u32_e32 v28, vcc, s2, v26
	global_load_dwordx4 v[2:5], v130, s[0:1] offset:1024 nt
	global_load_dwordx4 v[6:9], v130, s[0:1] offset:2048 nt
	v_addc_co_u32_e32 v29, vcc, 0, v27, vcc
	global_load_dwordx4 v[10:13], v130, s[0:1] offset:3072 nt
	global_load_dwordx4 v[14:17], v[28:29], off offset:-4096 nt
	global_load_dwordx4 v[18:21], v[66:67], off offset:1024 nt
	global_load_dwordx4 v[22:25], v[66:67], off offset:2048 nt
	global_load_dwordx4 v[30:33], v[28:29], off nt
	global_load_dwordx4 v[34:37], v[28:29], off offset:1024 nt
	global_load_dwordx4 v[42:45], v[28:29], off offset:2048 nt
	global_load_dwordx4 v[46:49], v[28:29], off offset:3072 nt
	s_movk_i32 s2, 0x3000
	v_add_co_u32_e32 v68, vcc, s2, v26
	v_mbcnt_lo_u32_b32 v1, -1, 0
	s_nop 0
	v_addc_co_u32_e32 v69, vcc, 0, v27, vcc
	global_load_dwordx4 v[38:41], v[66:67], off offset:3072 nt
	global_load_dwordx4 v[50:53], v[68:69], off nt
	global_load_dwordx4 v[54:57], v[68:69], off offset:1024 nt
	global_load_dwordx4 v[58:61], v[68:69], off offset:2048 nt
	global_load_dwordx4 v[26:29], v130, s[0:1] nt
	global_load_dwordx4 v[62:65], v[68:69], off offset:3072 nt
	v_mbcnt_hi_u32_b32 v66, -1, v1
	v_and_b32_e32 v1, 64, v66
	v_add_u32_e32 v67, 64, v1
	v_xor_b32_e32 v1, 1, v66
	v_cmp_lt_i32_e32 vcc, v1, v67
	v_xor_b32_e32 v68, 2, v66
	s_lshl_b32 s0, s94, 15
	v_cndmask_b32_e32 v1, v66, v1, vcc
	v_cmp_lt_i32_e32 vcc, v68, v67
	s_lshl_b32 s1, s10, 12
	s_add_i32 s0, s0, s1
	v_cndmask_b32_e32 v68, v66, v68, vcc
	v_lshlrev_b32_e32 v136, 2, v68
	v_xor_b32_e32 v68, 4, v66
	v_cmp_lt_i32_e32 vcc, v68, v67
	v_readlane_b32 s1, v245, 7
	s_lshl_b32 s1, s1, 12
	v_cndmask_b32_e32 v68, v66, v68, vcc
	v_lshlrev_b32_e32 v137, 2, v68
	v_xor_b32_e32 v68, 8, v66
	v_cmp_lt_i32_e32 vcc, v68, v67
	v_lshlrev_b32_e32 v1, 2, v1
	s_lshl_b32 s16, s96, 4
	v_cndmask_b32_e32 v68, v66, v68, vcc
	v_lshlrev_b32_e32 v138, 2, v68
	v_xor_b32_e32 v68, 16, v66
	v_cmp_lt_i32_e32 vcc, v68, v67
	s_lshl_b32 s17, s96, 16
	s_add_i32 s10, s0, s1
	v_cndmask_b32_e32 v68, v66, v68, vcc
	v_lshlrev_b32_e32 v139, 2, v68
	v_xor_b32_e32 v68, 32, v66
	v_cmp_lt_i32_e32 vcc, v68, v67
	s_lshl_b32 s18, s96, 15
	s_mov_b32 s19, 0x42fe0000
	v_cndmask_b32_e32 v66, v66, v68, vcc
	v_lshlrev_b32_e32 v140, 2, v66
	s_mov_b32 s20, 0x40c0c00
	s_mov_b32 s21, 0x400000
	s_mov_b32 s22, 0x800000
	s_mov_b32 s23, 0xc00000
	s_mov_b32 s24, 0x1000000
	s_mov_b32 s25, 0x1400000
	s_mov_b32 s26, 0x1800000
	s_mov_b32 s27, 0x1c00000
	s_brev_b32 s28, 64
	s_mov_b32 s29, 0x2400000
	s_mov_b32 s30, 0x2800000
	s_mov_b32 s31, 0x2c00000
	s_mov_b32 s34, 0x3000000
	s_mov_b32 s35, 0x3400000
	s_mov_b32 s36, 0x3800000
	s_brev_b32 s37, 16
	s_branch .LBB0_229

; __device__ __forceinline__ void pt_load(const float* tu, const float* tv, f32x4* v, int r, int lane) {
;     const f32x4* sp = (const f32x4*)(((r >> 14) ? tv : tu) + (size_t)(r & 16383) * D) + lane;
; #pragma unroll
;     for (int j = 0; j < 16; ++j) v[j] = sp[64 * j];
; }
; __device__ __forceinline__ void phase_peer_tables(const Frame& F, const Args& a, int r_lo, int r_hi, int gw, int NGW) {
;     ...
;         const int r1 = r + NGW; const bool h1 = r1 < r_hi;
;         if (h1) pt_load(a.in[17], a.in[18], vB, r1, lane);
.LBB0_229:
	s_add_i32 s38, s39, s9
	s_cmp_lt_i32 s38, s8
	s_cselect_b64 s[0:1], -1, 0
	s_cmp_ge_i32 s38, s8
	s_cbranch_scc1 .LBB0_231
	s_cmpk_lt_u32 s38, 0x4000
	s_cselect_b32 s3, s13, s15
	s_cselect_b32 s2, s12, s14
	s_add_i32 s4, s18, s10
	s_and_b32 s4, s4, 0x3fff000
	s_lshl_b32 s4, s4, 2
	s_add_u32 s2, s2, s4
	s_addc_u32 s3, s3, 0
	v_mov_b32_e32 v131, v133
	v_lshl_add_u64 v[114:115], s[2:3], 0, v[130:131]
	v_add_co_u32_e32 v82, vcc, s11, v114
	global_load_dwordx4 v[78:81], v130, s[2:3] nt
	global_load_dwordx4 v[74:77], v130, s[2:3] offset:1024 nt
	global_load_dwordx4 v[70:73], v130, s[2:3] offset:2048 nt
	global_load_dwordx4 v[66:69], v130, s[2:3] offset:3072 nt
	v_addc_co_u32_e32 v83, vcc, 0, v115, vcc
	v_add_co_u32_e32 v98, vcc, 0x2000, v114
	global_load_dwordx4 v[94:97], v[82:83], off nt
	global_load_dwordx4 v[90:93], v[82:83], off offset:1024 nt
	global_load_dwordx4 v[86:89], v[82:83], off offset:2048 nt
	s_nop 0
	global_load_dwordx4 v[82:85], v[82:83], off offset:3072 nt
	v_addc_co_u32_e32 v99, vcc, 0, v115, vcc
	v_add_co_u32_e32 v114, vcc, 0x3000, v114
	global_load_dwordx4 v[110:113], v[98:99], off nt
	global_load_dwordx4 v[106:109], v[98:99], off offset:1024 nt
	global_load_dwordx4 v[102:105], v[98:99], off offset:2048 nt
	s_nop 0
	global_load_dwordx4 v[98:101], v[98:99], off offset:3072 nt
	v_addc_co_u32_e32 v115, vcc, 0, v115, vcc
	global_load_dwordx4 v[126:129], v[114:115], off nt
	global_load_dwordx4 v[122:125], v[114:115], off offset:1024 nt
	global_load_dwordx4 v[118:121], v[114:115], off offset:2048 nt
	s_nop 0
	global_load_dwordx4 v[114:117], v[114:115], off offset:3072 nt

; __device__ __forceinline__ void pt_load(const float* tu, const float* tv, f32x4* v, int r, int lane) {
;     const f32x4* sp = (const f32x4*)(((r >> 14) ? tv : tu) + (size_t)(r & 16383) * D) + lane;
; #pragma unroll
;     for (int j = 0; j < 16; ++j) v[j] = sp[64 * j];
; }
; __device__ __forceinline__ void phase_peer_tables(const Frame& F, const Args& a, int r_lo, int r_hi, int gw, int NGW) {
;     ...
;         const int r2 = r1 + NGW; const bool h2 = r2 < r_hi;
;         if (h2) pt_load(a.in[17], a.in[18], vA, r2, lane);
.LBB0_234:
	s_add_i32 s0, s16, s39
	s_cmp_ge_i32 s0, s8
	s_cbranch_scc1 .LBB0_236
	s_cmpk_lt_u32 s0, 0x4000
	s_cselect_b32 s1, s13, s15
	s_cselect_b32 s0, s12, s14
	s_add_i32 s2, s17, s10
	s_and_b32 s2, s2, 0x3fff000
	s_lshl_b32 s2, s2, 2
	s_add_u32 s0, s0, s2
	s_addc_u32 s1, s1, 0
	v_mov_b32_e32 v131, v133
	v_lshl_add_u64 v[50:51], s[0:1], 0, v[130:131]
	v_add_co_u32_e32 v30, vcc, s11, v50
	global_load_dwordx4 v[26:29], v130, s[0:1] nt
	global_load_dwordx4 v[2:5], v130, s[0:1] offset:1024 nt
	global_load_dwordx4 v[6:9], v130, s[0:1] offset:2048 nt
	global_load_dwordx4 v[10:13], v130, s[0:1] offset:3072 nt
	v_addc_co_u32_e32 v31, vcc, 0, v51, vcc
	v_add_co_u32_e32 v46, vcc, 0x2000, v50
	global_load_dwordx4 v[14:17], v[30:31], off nt
	global_load_dwordx4 v[18:21], v[30:31], off offset:1024 nt
	global_load_dwordx4 v[22:25], v[30:31], off offset:2048 nt
	global_load_dwordx4 v[38:41], v[30:31], off offset:3072 nt
	v_addc_co_u32_e32 v47, vcc, 0, v51, vcc
	v_add_co_u32_e32 v62, vcc, 0x3000, v50
	global_load_dwordx4 v[30:33], v[46:47], off nt
	global_load_dwordx4 v[34:37], v[46:47], off offset:1024 nt
	global_load_dwordx4 v[42:45], v[46:47], off offset:2048 nt
	s_nop 0
	global_load_dwordx4 v[46:49], v[46:47], off offset:3072 nt
	v_addc_co_u32_e32 v63, vcc, 0, v51, vcc
	global_load_dwordx4 v[50:53], v[62:63], off nt
	global_load_dwordx4 v[54:57], v[62:63], off offset:1024 nt
	global_load_dwordx4 v[58:61], v[62:63], off offset:2048 nt
	s_nop 0
	global_load_dwordx4 v[62:65], v[62:63], off offset:3072 nt

; __device__ __forceinline__ void pt_load(const float* tu, const float* tv, f32x4* v, int r, int lane) {
;     const f32x4* sp = (const f32x4*)(((r >> 14) ? tv : tu) + (size_t)(r & 16383) * D) + lane;
; #pragma unroll
;     for (int j = 0; j < 16; ++j) v[j] = sp[64 * j];
; }
; __device__ __forceinline__ void phase_peer_tables(const Frame& F, const Args& a, int r_lo, int r_hi, int gw, int NGW) {
;     unsigned char* PT = a.ws + WS_PT; const int lane = F.lane;
;     int r = r_lo + gw; if (r >= r_hi) return;
;     f32x4 vA[16], vB[16];
;     pt_load(a.in[17], a.in[18], vA, r, lane);
.Lpt3_entry:
	s_load_dwordx4 s[12:15], s[86:87], 0x88
	s_load_dwordx2 s[2:3], s[86:87], 0xc0
	s_sub_i32 s45, s94, 64
	s_movk_i32 s44, 0xc0
	s_lshl_b32 s0, s45, 3
	v_readlane_b32 s1, v245, 7
	s_add_i32 s4, s1, s0
	s_movk_i32 s0, 0x600
	v_cmp_eq_u32_e64 s[6:7], 0, v194
	s_waitcnt vmcnt(0) lgkmcnt(0)
	s_movk_i32 s5, 0x7000
	s_add_i32 s41, s5, s4
	s_cmpk_gt_i32 s41, 0x7fff
	s_movk_i32 s4, 0x3000
	s_cbranch_scc1 .Lpt3_end
	s_add_u32 s1, s2, 0x3ba00000
	s_addc_u32 s10, s3, 0
	s_cmpk_lt_u32 s41, 0x4000
	s_cselect_b32 s3, s13, s15
	s_cselect_b32 s2, s12, s14
	s_lshl_b32 s8, s41, 14
	s_and_b32 s8, s8, 0xfffc000
	s_add_u32 s2, s2, s8
	v_mov_b32_e32 v133, 0
	s_addc_u32 s3, s3, 0
	v_lshlrev_b32_e32 v130, 4, v194
	v_mov_b32_e32 v131, v133
	v_lshl_add_u64 v[26:27], s[2:3], 0, v[130:131]
	s_movk_i32 s11, 0x1000
	v_add_co_u32_e32 v66, vcc, s11, v26
	s_movk_i32 s8, 0x2000
	s_nop 0
	v_addc_co_u32_e32 v67, vcc, 0, v27, vcc
	v_add_co_u32_e32 v28, vcc, s8, v26
	global_load_dwordx4 v[2:5], v130, s[2:3] offset:1024 nt
	global_load_dwordx4 v[6:9], v130, s[2:3] offset:2048 nt
	v_addc_co_u32_e32 v29, vcc, 0, v27, vcc
	global_load_dwordx4 v[10:13], v130, s[2:3] offset:3072 nt
	global_load_dwordx4 v[14:17], v[28:29], off offset:-4096 nt
	global_load_dwordx4 v[18:21], v[66:67], off offset:1024 nt
	global_load_dwordx4 v[22:25], v[66:67], off offset:2048 nt
	global_load_dwordx4 v[30:33], v[28:29], off nt
	global_load_dwordx4 v[38:41], v[28:29], off offset:1024 nt
	global_load_dwordx4 v[42:45], v[28:29], off offset:2048 nt
	global_load_dwordx4 v[46:49], v[28:29], off offset:3072 nt
	v_add_co_u32_e32 v68, vcc, s4, v26
	v_mbcnt_lo_u32_b32 v1, -1, 0
	s_nop 0
	v_addc_co_u32_e32 v69, vcc, 0, v27, vcc
	global_load_dwordx4 v[34:37], v[66:67], off offset:3072 nt
	global_load_dwordx4 v[50:53], v[68:69], off nt
	global_load_dwordx4 v[54:57], v[68:69], off offset:1024 nt
	global_load_dwordx4 v[58:61], v[68:69], off offset:2048 nt
	global_load_dwordx4 v[26:29], v130, s[2:3] nt
	global_load_dwordx4 v[62:65], v[68:69], off offset:3072 nt
	v_mbcnt_hi_u32_b32 v66, -1, v1
	v_and_b32_e32 v1, 64, v66
	v_add_u32_e32 v67, 64, v1
	v_xor_b32_e32 v1, 1, v66
	v_cmp_lt_i32_e32 vcc, v1, v67
	v_xor_b32_e32 v68, 2, v66
	s_lshl_b32 s2, s45, 15
	v_cndmask_b32_e32 v1, v66, v1, vcc
	v_cmp_lt_i32_e32 vcc, v68, v67
	s_lshl_b32 s3, s5, 12
	s_add_i32 s2, s2, s3
	v_cndmask_b32_e32 v68, v66, v68, vcc
	v_lshlrev_b32_e32 v136, 2, v68
	v_xor_b32_e32 v68, 4, v66
	v_cmp_lt_i32_e32 vcc, v68, v67
	v_readlane_b32 s3, v245, 7
	s_lshl_b32 s3, s3, 12
	v_cndmask_b32_e32 v68, v66, v68, vcc
	v_lshlrev_b32_e32 v137, 2, v68
	v_xor_b32_e32 v68, 8, v66
	v_cmp_lt_i32_e32 vcc, v68, v67
	v_lshlrev_b32_e32 v1, 2, v1
	s_lshl_b32 s16, s44, 4
	v_cndmask_b32_e32 v68, v66, v68, vcc
	v_lshlrev_b32_e32 v138, 2, v68
	v_xor_b32_e32 v68, 16, v66
	v_cmp_lt_i32_e32 vcc, v68, v67
	s_lshl_b32 s17, s44, 16
	s_add_i32 s20, s2, s3
	v_cndmask_b32_e32 v68, v66, v68, vcc
	v_lshlrev_b32_e32 v139, 2, v68
	v_xor_b32_e32 v68, 32, v66
	v_cmp_lt_i32_e32 vcc, v68, v67
	s_lshl_b32 s21, s44, 15
	s_mov_b32 s22, 0x42fe0000
	v_cndmask_b32_e32 v66, v66, v68, vcc
	v_lshlrev_b32_e32 v140, 2, v66
	s_mov_b32 s23, 0x40c0c00
	s_mov_b32 s24, 0x400000
	s_mov_b32 s25, 0x800000
	s_mov_b32 s26, 0xc00000
	s_mov_b32 s27, 0x1000000
	s_mov_b32 s28, 0x1400000
	s_mov_b32 s29, 0x1800000
	s_mov_b32 s30, 0x1c00000
	s_brev_b32 s31, 64
	s_mov_b32 s33, 0x2400000
	s_mov_b32 s34, 0x2800000
	s_mov_b32 s35, 0x2c00000
	s_mov_b32 s36, 0x3000000
	s_mov_b32 s37, 0x3400000
	s_mov_b32 s38, 0x3800000
	s_brev_b32 s39, 16
	s_branch .Lpt3_1252

; __device__ __forceinline__ void pt_load(const float* tu, const float* tv, f32x4* v, int r, int lane) {
;     const f32x4* sp = (const f32x4*)(((r >> 14) ? tv : tu) + (size_t)(r & 16383) * D) + lane;
; #pragma unroll
;     for (int j = 0; j < 16; ++j) v[j] = sp[64 * j];
; }
; __device__ __forceinline__ void phase_peer_tables(const Frame& F, const Args& a, int r_lo, int r_hi, int gw, int NGW) {
;     ...
;         const int r1 = r + NGW; const bool h1 = r1 < r_hi;
;         if (h1) pt_load(a.in[17], a.in[18], vB, r1, lane);
.Lpt3_1252:
	s_add_i32 s40, s41, s0
	s_cmp_lt_i32 s40, 0x8000
	s_cselect_b64 s[2:3], -1, 0
	s_cmpk_gt_i32 s40, 0x7fff
	s_cbranch_scc1 .Lpt3_1254
	s_cmpk_lt_u32 s40, 0x4000
	s_cselect_b32 s5, s13, s15
	s_cselect_b32 s4, s12, s14
	s_add_i32 s8, s21, s20
	s_and_b32 s8, s8, 0x3fff000
	s_lshl_b32 s8, s8, 2
	s_add_u32 s4, s4, s8
	s_addc_u32 s5, s5, 0
	v_mov_b32_e32 v131, v133
	v_lshl_add_u64 v[114:115], s[4:5], 0, v[130:131]
	v_add_co_u32_e32 v82, vcc, s11, v114
	global_load_dwordx4 v[78:81], v130, s[4:5] nt
	global_load_dwordx4 v[74:77], v130, s[4:5] offset:1024 nt
	global_load_dwordx4 v[70:73], v130, s[4:5] offset:2048 nt
	global_load_dwordx4 v[66:69], v130, s[4:5] offset:3072 nt
	v_addc_co_u32_e32 v83, vcc, 0, v115, vcc
	v_add_co_u32_e32 v98, vcc, 0x2000, v114
	global_load_dwordx4 v[94:97], v[82:83], off nt
	global_load_dwordx4 v[90:93], v[82:83], off offset:1024 nt
	global_load_dwordx4 v[86:89], v[82:83], off offset:2048 nt
	s_nop 0
	global_load_dwordx4 v[82:85], v[82:83], off offset:3072 nt
	v_addc_co_u32_e32 v99, vcc, 0, v115, vcc
	v_add_co_u32_e32 v114, vcc, 0x3000, v114
	global_load_dwordx4 v[110:113], v[98:99], off nt
	global_load_dwordx4 v[106:109], v[98:99], off offset:1024 nt
	global_load_dwordx4 v[102:105], v[98:99], off offset:2048 nt
	s_nop 0
	global_load_dwordx4 v[98:101], v[98:99], off offset:3072 nt
	v_addc_co_u32_e32 v115, vcc, 0, v115, vcc
	global_load_dwordx4 v[126:129], v[114:115], off nt
	global_load_dwordx4 v[122:125], v[114:115], off offset:1024 nt
	global_load_dwordx4 v[118:121], v[114:115], off offset:2048 nt
	s_nop 0
	global_load_dwordx4 v[114:117], v[114:115], off offset:3072 nt

; __device__ __forceinline__ void pt_load(const float* tu, const float* tv, f32x4* v, int r, int lane) {
;     const f32x4* sp = (const f32x4*)(((r >> 14) ? tv : tu) + (size_t)(r & 16383) * D) + lane;
; #pragma unroll
;     for (int j = 0; j < 16; ++j) v[j] = sp[64 * j];
; }
; __device__ __forceinline__ void phase_peer_tables(const Frame& F, const Args& a, int r_lo, int r_hi, int gw, int NGW) {
;     ...
;         const int r2 = r1 + NGW; const bool h2 = r2 < r_hi;
;         if (h2) pt_load(a.in[17], a.in[18], vA, r2, lane);
.Lpt3_1257:
	s_add_i32 s2, s16, s41
	s_cmpk_gt_i32 s2, 0x7fff
	s_cbranch_scc1 .Lpt3_1259
	s_cmpk_lt_u32 s2, 0x4000
	s_cselect_b32 s3, s13, s15
	s_cselect_b32 s2, s12, s14
	s_add_i32 s4, s17, s20
	s_and_b32 s4, s4, 0x3fff000
	s_lshl_b32 s4, s4, 2
	s_add_u32 s2, s2, s4
	s_addc_u32 s3, s3, 0
	v_mov_b32_e32 v131, v133
	v_lshl_add_u64 v[50:51], s[2:3], 0, v[130:131]
	v_add_co_u32_e32 v30, vcc, s11, v50
	global_load_dwordx4 v[26:29], v130, s[2:3] nt
	global_load_dwordx4 v[2:5], v130, s[2:3] offset:1024 nt
	global_load_dwordx4 v[6:9], v130, s[2:3] offset:2048 nt
	global_load_dwordx4 v[10:13], v130, s[2:3] offset:3072 nt
	v_addc_co_u32_e32 v31, vcc, 0, v51, vcc
	v_add_co_u32_e32 v46, vcc, 0x2000, v50
	global_load_dwordx4 v[14:17], v[30:31], off nt
	global_load_dwordx4 v[18:21], v[30:31], off offset:1024 nt
	global_load_dwordx4 v[22:25], v[30:31], off offset:2048 nt
	global_load_dwordx4 v[34:37], v[30:31], off offset:3072 nt
	v_addc_co_u32_e32 v47, vcc, 0, v51, vcc
	v_add_co_u32_e32 v62, vcc, 0x3000, v50
	global_load_dwordx4 v[30:33], v[46:47], off nt
	global_load_dwordx4 v[38:41], v[46:47], off offset:1024 nt
	global_load_dwordx4 v[42:45], v[46:47], off offset:2048 nt
	s_nop 0
	global_load_dwordx4 v[46:49], v[46:47], off offset:3072 nt
	v_addc_co_u32_e32 v63, vcc, 0, v51, vcc
	global_load_dwordx4 v[50:53], v[62:63], off nt
	global_load_dwordx4 v[54:57], v[62:63], off offset:1024 nt
	global_load_dwordx4 v[58:61], v[62:63], off offset:2048 nt
	s_nop 0
	global_load_dwordx4 v[62:65], v[62:63], off offset:3072 nt
